# sparse attention: gathers via SGPR base + 32-bit offsets (drops 13 u64 adds per step) and bias-offset LDS reads of tile jt+1 issued under tile jt's MFMAs; on top of band running addresses
# baseline (speedup 1.0000x reference)
.LBB0_1382:
	s_or_b64 exec, exec, s[0:1]
	ds_write_b128 v242, v[140:143] offset:10496
	ds_write_b128 v242, v[160:163] offset:11520
	s_waitcnt lgkmcnt(0)
	v_add_u32_e32 v170, 0x2800, v243
	ds_read2_b32 v[162:163], v170 offset0:64 offset1:80
	ds_read2_b32 v[166:167], v170 offset0:96 offset1:112
	ds_read2_b32 v[168:169], v170 offset0:128 offset1:144
	ds_read2_b32 v[170:171], v170 offset0:160 offset1:176
	v_add_u32_e32 v186, 0x2800, v244
	s_waitcnt lgkmcnt(3)
	v_add_u32_e32 v160, v162, v208
	v_add_u32_e32 v162, v163, v208
	s_waitcnt lgkmcnt(2)
	v_add_u32_e32 v164, v166, v208
	v_add_u32_e32 v166, v167, v208
	s_waitcnt lgkmcnt(1)
	v_add_u32_e32 v178, v168, v208
	v_add_u32_e32 v180, v169, v208
	ds_read2_b32 v[168:169], v186 offset0:64 offset1:80
	s_waitcnt lgkmcnt(1)
	v_add_u32_e32 v182, v170, v208
	v_add_u32_e32 v184, v171, v208
	ds_read2_b32 v[170:171], v186 offset0:96 offset1:112
	s_waitcnt lgkmcnt(1)
	v_add_u32_e32 v186, v168, v209
	ds_read_b32 v168, v244 offset:10752
	v_add_u32_e32 v188, v169, v209
	s_waitcnt lgkmcnt(1)
	v_add_u32_e32 v190, v170, v209
	v_add_u32_e32 v192, v171, v209
	s_waitcnt lgkmcnt(0)
	v_add_u32_e32 v194, v168, v209
	s_mov_b64 s[30:31], -1
.LBB0_1383:
	s_and_b64 vcc, exec, s[28:29]
	s_mov_b64 s[0:1], s[20:21]
	s_mov_b32 s47, s43
	s_cbranch_vccz .LBB0_1385
	v_add_u32_e32 v2, s42, v207
	v_add_u32_e32 v160, 0x2800, v2
	ds_read2_b32 v[162:163], v160 offset0:192 offset1:208
	v_add_u32_e32 v170, 0x2c00, v2
	ds_read2_b32 v[166:167], v160 offset0:224 offset1:240
	ds_read2_b32 v[168:169], v170 offset1:16
	ds_read2_b32 v[170:171], v170 offset0:32 offset1:48
	v_add_u32_e32 v186, 0x2800, v245
	s_waitcnt lgkmcnt(3)
	v_add_u32_e32 v160, v162, v208
	v_add_u32_e32 v162, v163, v208
	s_waitcnt lgkmcnt(2)
	v_add_u32_e32 v164, v166, v208
	v_add_u32_e32 v166, v167, v208
	s_waitcnt lgkmcnt(1)
	v_add_u32_e32 v178, v168, v208
	v_add_u32_e32 v180, v169, v208
	ds_read2_b32 v[168:169], v186 offset0:192 offset1:208
	s_waitcnt lgkmcnt(1)
	v_add_u32_e32 v182, v170, v208
	v_add_u32_e32 v184, v171, v208
	ds_read2_b32 v[170:171], v186 offset0:224 offset1:240
	s_waitcnt lgkmcnt(1)
	v_add_u32_e32 v186, v168, v209
	ds_read_b32 v168, v245 offset:11264
	v_add_u32_e32 v188, v169, v209
	s_waitcnt lgkmcnt(1)
	v_add_u32_e32 v190, v170, v209
	v_add_u32_e32 v192, v171, v209
	s_waitcnt lgkmcnt(0)
	v_add_u32_e32 v194, v168, v209
	s_mov_b64 s[30:31], -1
	s_mov_b64 s[0:1], s[24:25]
	s_mov_b32 s47, s45
.LBB0_1385:
	s_andn2_b64 vcc, exec, s[30:31]
	s_mov_b64 s[28:29], 0
	s_cbranch_vccnz .LBB0_1387
	v_lshl_add_u32 v2, v210, 2, s47
	ds_read2_b32 v[68:69], v2 offset0:80 offset1:96
	s_add_u32 s0, s35, s0
	s_addc_u32 s1, s36, s1
	global_load_dwordx4 v[100:103], v186, s[0:1]
	s_mov_b64 s[28:29], -1
	s_waitcnt lgkmcnt(0)
	v_add_u32_e32 v68, v68, v209
	v_add_u32_e32 v69, v69, v209
	global_load_dwordx4 v[124:127], v188, s[0:1]
	global_load_dwordx4 v[120:123], v190, s[0:1]
	global_load_dwordx4 v[116:119], v192, s[0:1]
	global_load_dwordx4 v[112:115], v194, s[0:1]
	global_load_dwordx4 v[108:111], v68, s[0:1]
	global_load_dwordx4 v[104:107], v69, s[0:1]
	global_load_dwordx4 v[80:83], v160, s[0:1]
	global_load_dwordx4 v[76:79], v162, s[0:1]
	global_load_dwordx4 v[72:75], v164, s[0:1]
	s_nop 0
	global_load_dwordx4 v[68:71], v166, s[0:1]
	ds_read_b32 v2, v2 offset:448
	global_load_dwordx4 v[96:99], v178, s[0:1]
	global_load_dwordx4 v[92:95], v180, s[0:1]
	global_load_dwordx4 v[88:91], v182, s[0:1]
	global_load_dwordx4 v[84:87], v184, s[0:1]
	s_waitcnt lgkmcnt(0)
	v_add_u32_e32 v2, v2, v209
	global_load_dwordx4 v[128:131], v2, s[0:1]
.LBB0_1387:
	ds_read_b128 v[160:163], v246
	s_andn2_b64 vcc, exec, s[28:29]
	s_waitcnt lgkmcnt(0)
	v_add_u32_e32 v2, v211, v160
	v_add_u32_e32 v160, v211, v161
	v_add_u32_e32 v161, v211, v162
	v_add_u32_e32 v162, v211, v163
	v_mfma_f32_16x16x32_fp8_fp8 v[164:167], v[8:9], v[174:175], 0
	ds_read_b32 v168, v2 offset:8192
	ds_read_b32 v169, v160 offset:8192
	ds_read_b32 v170, v161 offset:8192
	ds_read_b32 v171, v162 offset:8192
	v_mfma_f32_16x16x32_fp8_fp8 v[160:163], v[10:11], v[176:177], v[164:167]
	ds_read_b128 v[164:167], v246 offset:64
	s_waitcnt lgkmcnt(1)
	s_nop 6
	v_pk_fma_f32 v[160:161], v[160:161], s[72:73], v[168:169] op_sel_hi:[1,0,1]
	v_pk_fma_f32 v[162:163], v[162:163], s[72:73], v[170:171] op_sel_hi:[1,0,1]
	s_waitcnt lgkmcnt(0)
	v_add_u32_e32 v2, v211, v164
	v_add_u32_e32 v169, v211, v165
	v_add_u32_e32 v170, v211, v166
	v_add_u32_e32 v171, v211, v167
	v_mfma_f32_16x16x32_fp8_fp8 v[164:167], v[4:5], v[174:175], 0
	ds_read_b32 v168, v2 offset:8192
	ds_read_b32 v169, v169 offset:8192
	ds_read_b32 v170, v170 offset:8192
	ds_read_b32 v171, v171 offset:8192
	v_mfma_f32_16x16x32_fp8_fp8 v[164:167], v[6:7], v[176:177], v[164:167]
	ds_read_b128 v[178:181], v246 offset:128
	s_waitcnt lgkmcnt(1)
	s_nop 6
	v_pk_fma_f32 v[164:165], v[164:165], s[72:73], v[168:169] op_sel_hi:[1,0,1]
	v_pk_fma_f32 v[166:167], v[166:167], s[72:73], v[170:171] op_sel_hi:[1,0,1]
	s_waitcnt lgkmcnt(0)
	v_add_u32_e32 v2, v211, v178
	v_add_u32_e32 v169, v211, v179
	v_add_u32_e32 v170, v211, v180
	v_add_u32_e32 v171, v211, v181
	v_mfma_f32_16x16x32_fp8_fp8 v[178:181], v[16:17], v[174:175], 0
	ds_read_b32 v168, v2 offset:8192
	ds_read_b32 v169, v169 offset:8192
	ds_read_b32 v170, v170 offset:8192
	ds_read_b32 v171, v171 offset:8192
	v_mfma_f32_16x16x32_fp8_fp8 v[178:181], v[18:19], v[176:177], v[178:181]
	ds_read_b128 v[182:185], v246 offset:192
	s_waitcnt lgkmcnt(1)
	s_nop 6
	v_pk_fma_f32 v[178:179], v[178:179], s[72:73], v[168:169] op_sel_hi:[1,0,1]
	v_pk_fma_f32 v[180:181], v[180:181], s[72:73], v[170:171] op_sel_hi:[1,0,1]
	s_waitcnt lgkmcnt(0)
	v_add_u32_e32 v2, v211, v182
	v_add_u32_e32 v169, v211, v183
	v_add_u32_e32 v170, v211, v184
	v_add_u32_e32 v171, v211, v185
	v_mfma_f32_16x16x32_fp8_fp8 v[182:185], v[12:13], v[174:175], 0
	ds_read_b32 v168, v2 offset:8192
	ds_read_b32 v169, v169 offset:8192
	ds_read_b32 v170, v170 offset:8192
	ds_read_b32 v171, v171 offset:8192
	v_mfma_f32_16x16x32_fp8_fp8 v[182:185], v[14:15], v[176:177], v[182:185]
	ds_read_b128 v[186:189], v246 offset:256
	s_waitcnt lgkmcnt(1)
	s_nop 6
	v_pk_fma_f32 v[182:183], v[182:183], s[72:73], v[168:169] op_sel_hi:[1,0,1]
	v_pk_fma_f32 v[184:185], v[184:185], s[72:73], v[170:171] op_sel_hi:[1,0,1]
	s_nop 0
	v_max3_f32 v2, v160, s33, v161
	v_max3_f32 v2, v2, v162, v163
	v_max3_f32 v2, v2, v164, v165
	v_max3_f32 v2, v2, v166, v167
	v_max3_f32 v2, v2, v178, v179
	v_max3_f32 v2, v2, v180, v181
	v_max3_f32 v2, v2, v182, v183
	v_max3_f32 v2, v2, v184, v185
	s_waitcnt lgkmcnt(0)
	v_add_u32_e32 v168, v211, v186
	v_add_u32_e32 v169, v211, v187
	v_add_u32_e32 v170, v211, v188
	v_add_u32_e32 v171, v211, v189
	v_mfma_f32_16x16x32_fp8_fp8 v[186:189], v[24:25], v[174:175], 0
	ds_read_b32 v168, v168 offset:8192
	ds_read_b32 v169, v169 offset:8192
	ds_read_b32 v170, v170 offset:8192
	ds_read_b32 v171, v171 offset:8192
	v_mfma_f32_16x16x32_fp8_fp8 v[186:189], v[26:27], v[176:177], v[186:189]
	ds_read_b128 v[190:193], v246 offset:320
	s_waitcnt lgkmcnt(1)
	s_nop 6
	v_pk_fma_f32 v[234:235], v[186:187], s[72:73], v[168:169] op_sel_hi:[1,0,1]
	v_pk_fma_f32 v[236:237], v[188:189], s[72:73], v[170:171] op_sel_hi:[1,0,1]
	s_nop 0
	v_max3_f32 v2, v2, v234, v235
	v_max3_f32 v2, v2, v236, v237
	s_waitcnt lgkmcnt(0)
	v_add_u32_e32 v168, v211, v190
	v_add_u32_e32 v169, v211, v191
	v_add_u32_e32 v170, v211, v192
	v_add_u32_e32 v171, v211, v193
	v_mfma_f32_16x16x32_fp8_fp8 v[186:189], v[20:21], v[174:175], 0
	ds_read_b32 v168, v168 offset:8192
	ds_read_b32 v169, v169 offset:8192
	ds_read_b32 v170, v170 offset:8192
	ds_read_b32 v171, v171 offset:8192
	v_mfma_f32_16x16x32_fp8_fp8 v[186:189], v[22:23], v[176:177], v[186:189]
	ds_read_b128 v[190:193], v246 offset:384
	s_waitcnt lgkmcnt(1)
	s_nop 6
	v_pk_fma_f32 v[228:229], v[186:187], s[72:73], v[168:169] op_sel_hi:[1,0,1]
	v_pk_fma_f32 v[230:231], v[188:189], s[72:73], v[170:171] op_sel_hi:[1,0,1]
	s_nop 0
	v_max3_f32 v2, v2, v228, v229
	v_max3_f32 v2, v2, v230, v231
	s_waitcnt lgkmcnt(0)
	v_add_u32_e32 v168, v211, v190
	v_add_u32_e32 v169, v211, v191
	v_add_u32_e32 v170, v211, v192
	v_add_u32_e32 v171, v211, v193
	v_mfma_f32_16x16x32_fp8_fp8 v[186:189], v[32:33], v[174:175], 0
	ds_read_b32 v168, v168 offset:8192
	ds_read_b32 v169, v169 offset:8192
	ds_read_b32 v170, v170 offset:8192
	ds_read_b32 v171, v171 offset:8192
	v_mfma_f32_16x16x32_fp8_fp8 v[186:189], v[34:35], v[176:177], v[186:189]
	ds_read_b128 v[190:193], v246 offset:448
	s_waitcnt lgkmcnt(1)
	s_nop 6
	v_pk_fma_f32 v[168:169], v[186:187], s[72:73], v[168:169] op_sel_hi:[1,0,1]
	v_pk_fma_f32 v[170:171], v[188:189], s[72:73], v[170:171] op_sel_hi:[1,0,1]
	s_nop 0
	v_max3_f32 v2, v2, v168, v169
	v_max3_f32 v2, v2, v170, v171
	s_waitcnt lgkmcnt(0)
	v_add_u32_e32 v190, v211, v190
	v_add_u32_e32 v191, v211, v191
	v_add_u32_e32 v192, v211, v192
	v_add_u32_e32 v193, v211, v193
	v_mfma_f32_16x16x32_fp8_fp8 v[186:189], v[28:29], v[174:175], 0
	ds_read_b32 v190, v190 offset:8192
	ds_read_b32 v191, v191 offset:8192
	ds_read_b32 v192, v192 offset:8192
	ds_read_b32 v193, v193 offset:8192
	v_mfma_f32_16x16x32_fp8_fp8 v[186:189], v[30:31], v[176:177], v[186:189]
	s_waitcnt lgkmcnt(0)
	s_nop 6
	v_pk_fma_f32 v[216:217], v[186:187], s[72:73], v[190:191] op_sel_hi:[1,0,1]
	v_pk_fma_f32 v[218:219], v[188:189], s[72:73], v[192:193] op_sel_hi:[1,0,1]
	s_nop 0
	v_max3_f32 v2, v2, v216, v217
	v_max3_f32 v2, v2, v218, v219
	v_mov_b32_e32 v186, v2
	s_nop 1
	v_permlane16_swap_b32_e32 v2, v186
	v_max_f32_e32 v186, v186, v186
	v_max_f32_e32 v2, v2, v2
	v_max_f32_e32 v2, v2, v186
	v_mov_b32_e32 v186, v2
	s_nop 1
	v_permlane32_swap_b32_e32 v2, v186
	v_max3_f32 v214, v196, v2, v186
	v_sub_f32_e32 v163, v163, v214
	v_sub_f32_e32 v162, v162, v214
	v_sub_f32_e32 v161, v161, v214
	v_sub_f32_e32 v160, v160, v214
	v_sub_f32_e32 v2, v196, v214
	v_exp_f32_e32 v196, v160
	v_exp_f32_e32 v197, v161
	v_exp_f32_e32 v198, v162
	v_exp_f32_e32 v199, v163
	v_sub_f32_e32 v163, v167, v214
	v_sub_f32_e32 v162, v166, v214
	v_sub_f32_e32 v161, v165, v214
	v_sub_f32_e32 v160, v164, v214
	v_sub_f32_e32 v167, v219, v214
	v_exp_f32_e32 v200, v160
	v_exp_f32_e32 v201, v161
	v_exp_f32_e32 v202, v162
	v_exp_f32_e32 v203, v163
	v_sub_f32_e32 v163, v181, v214
	v_sub_f32_e32 v162, v180, v214
	v_sub_f32_e32 v161, v179, v214
	v_sub_f32_e32 v160, v178, v214
	v_sub_f32_e32 v166, v218, v214
	v_exp_f32_e32 v188, v160
	v_exp_f32_e32 v189, v161
	v_exp_f32_e32 v190, v162
	v_exp_f32_e32 v191, v163
	v_sub_f32_e32 v163, v185, v214
	v_sub_f32_e32 v162, v184, v214
	v_sub_f32_e32 v161, v183, v214
	v_sub_f32_e32 v160, v182, v214
	v_sub_f32_e32 v165, v217, v214
	v_exp_f32_e32 v192, v160
	v_exp_f32_e32 v193, v161
	v_exp_f32_e32 v194, v162
	v_exp_f32_e32 v195, v163
	v_sub_f32_e32 v163, v237, v214
	v_sub_f32_e32 v162, v236, v214
	v_sub_f32_e32 v161, v235, v214
	v_sub_f32_e32 v160, v234, v214
	v_sub_f32_e32 v164, v216, v214
	v_exp_f32_e32 v178, v160
	v_exp_f32_e32 v179, v161
	v_exp_f32_e32 v180, v162
	v_exp_f32_e32 v181, v163
	v_sub_f32_e32 v163, v231, v214
	v_sub_f32_e32 v162, v230, v214
	v_sub_f32_e32 v161, v229, v214
	v_sub_f32_e32 v160, v228, v214
	v_pk_add_f32 v[218:219], v[190:191], v[194:195]
	v_exp_f32_e32 v182, v160
	v_exp_f32_e32 v183, v161
	v_exp_f32_e32 v184, v162
	v_exp_f32_e32 v185, v163
	v_sub_f32_e32 v163, v171, v214
	v_sub_f32_e32 v162, v170, v214
	v_sub_f32_e32 v161, v169, v214
	v_sub_f32_e32 v160, v168, v214
	v_pk_add_f32 v[170:171], v[198:199], v[202:203]
	v_exp_f32_e32 v160, v160
	v_exp_f32_e32 v161, v161
	v_exp_f32_e32 v162, v162
	v_exp_f32_e32 v163, v163
	v_exp_f32_e32 v164, v164
	v_exp_f32_e32 v165, v165
	v_exp_f32_e32 v166, v166
	v_exp_f32_e32 v167, v167
	v_pk_add_f32 v[168:169], v[196:197], v[200:201]
	v_pk_add_f32 v[216:217], v[188:189], v[192:193]
	v_pk_add_f32 v[230:231], v[180:181], v[184:185]
	v_pk_add_f32 v[228:229], v[178:179], v[182:183]
	v_pk_add_f32 v[236:237], v[162:163], v[166:167]
	v_pk_add_f32 v[234:235], v[160:161], v[164:165]
	v_exp_f32_e32 v2, v2
	s_nop 0
	v_pk_add_f32 v[170:171], v[170:171], v[218:219]
	v_pk_add_f32 v[168:169], v[168:169], v[216:217]
	v_pk_add_f32 v[218:219], v[230:231], v[236:237]
	v_pk_add_f32 v[216:217], v[228:229], v[234:235]
	v_pk_mul_f32 v[158:159], v[158:159], v[2:3] op_sel_hi:[1,0]
	v_pk_mul_f32 v[156:157], v[156:157], v[2:3] op_sel_hi:[1,0]
	v_pk_add_f32 v[170:171], v[170:171], v[218:219]
	v_pk_add_f32 v[168:169], v[168:169], v[216:217]
	v_cvt_scalef32_pk_bf16_fp8 v217, v42, 1.0 op_sel:[1,0,0]
	v_cvt_scalef32_pk_bf16_fp8 v216, v42, 1.0
	v_pk_add_f32 v[186:187], v[168:169], v[170:171]
	v_cvt_scalef32_pk_bf16_fp8 v169, v40, 1.0 op_sel:[1,0,0]
	v_cvt_scalef32_pk_bf16_fp8 v168, v40, 1.0
	v_cvt_scalef32_pk_bf16_fp8 v171, v41, 1.0 op_sel:[1,0,0]
	v_cvt_scalef32_pk_bf16_fp8 v170, v41, 1.0
	v_cvt_scalef32_pk_bf16_fp8 v218, v43, 1.0
	v_cvt_scalef32_pk_bf16_fp8 v219, v43, 1.0 op_sel:[1,0,0]
	ds_write_b128 v220, v[168:171] offset:43264
	ds_write_b128 v220, v[216:219] offset:43280
	v_cvt_scalef32_pk_bf16_fp8 v169, v36, 1.0 op_sel:[1,0,0]
	v_cvt_scalef32_pk_bf16_fp8 v168, v36, 1.0
	v_cvt_scalef32_pk_bf16_fp8 v171, v37, 1.0 op_sel:[1,0,0]
	v_cvt_scalef32_pk_bf16_fp8 v170, v37, 1.0
	v_cvt_scalef32_pk_bf16_fp8 v217, v38, 1.0 op_sel:[1,0,0]
	v_cvt_scalef32_pk_bf16_fp8 v216, v38, 1.0
	v_cvt_scalef32_pk_bf16_fp8 v218, v39, 1.0
	v_cvt_scalef32_pk_bf16_fp8 v219, v39, 1.0 op_sel:[1,0,0]
	ds_write_b128 v220, v[168:171] offset:43776
	ds_write_b128 v220, v[216:219] offset:43792
	v_cvt_scalef32_pk_bf16_fp8 v169, v48, 1.0 op_sel:[1,0,0]
	v_cvt_scalef32_pk_bf16_fp8 v168, v48, 1.0
	v_cvt_scalef32_pk_bf16_fp8 v171, v49, 1.0 op_sel:[1,0,0]
	v_cvt_scalef32_pk_bf16_fp8 v170, v49, 1.0
	v_cvt_scalef32_pk_bf16_fp8 v217, v50, 1.0 op_sel:[1,0,0]
	v_cvt_scalef32_pk_bf16_fp8 v216, v50, 1.0
	v_cvt_scalef32_pk_bf16_fp8 v218, v51, 1.0
	v_cvt_scalef32_pk_bf16_fp8 v219, v51, 1.0 op_sel:[1,0,0]
	ds_write_b128 v220, v[168:171] offset:44288
	ds_write_b128 v220, v[216:219] offset:44304
	v_cvt_scalef32_pk_bf16_fp8 v169, v44, 1.0 op_sel:[1,0,0]
	v_cvt_scalef32_pk_bf16_fp8 v168, v44, 1.0
	v_cvt_scalef32_pk_bf16_fp8 v171, v45, 1.0 op_sel:[1,0,0]
	v_cvt_scalef32_pk_bf16_fp8 v170, v45, 1.0
	v_cvt_scalef32_pk_bf16_fp8 v217, v46, 1.0 op_sel:[1,0,0]
	v_cvt_scalef32_pk_bf16_fp8 v216, v46, 1.0
	v_cvt_scalef32_pk_bf16_fp8 v218, v47, 1.0
	v_cvt_scalef32_pk_bf16_fp8 v219, v47, 1.0 op_sel:[1,0,0]
	ds_write_b128 v220, v[168:171] offset:44800
	ds_write_b128 v220, v[216:219] offset:44816
	v_cvt_pk_bf16_f32 v168, v196, v197
	v_cvt_pk_bf16_f32 v169, v198, v199
	v_cvt_pk_bf16_f32 v170, v200, v201
	v_cvt_pk_bf16_f32 v171, v202, v203
	ds_read_b64_tr_b16 v[196:197], v221 offset:43264
	ds_read_b64_tr_b16 v[198:199], v221 offset:43776
	ds_read_b64_tr_b16 v[200:201], v221 offset:45312
	ds_read_b64_tr_b16 v[202:203], v221 offset:45824
	ds_read_b64_tr_b16 v[216:217], v221 offset:47360
	ds_read_b64_tr_b16 v[218:219], v221 offset:47872
	s_waitcnt lgkmcnt(4)
	v_mfma_f32_16x16x32_bf16 v[156:159], v[196:199], v[168:171], v[156:159]
	ds_read_b64_tr_b16 v[196:197], v221 offset:49408
	ds_read_b64_tr_b16 v[198:199], v221 offset:49920
	v_pk_mul_f32 v[154:155], v[154:155], v[2:3] op_sel_hi:[1,0]
	v_pk_mul_f32 v[152:153], v[152:153], v[2:3] op_sel_hi:[1,0]
	v_pk_mul_f32 v[150:151], v[150:151], v[2:3] op_sel_hi:[1,0]
	v_pk_mul_f32 v[148:149], v[148:149], v[2:3] op_sel_hi:[1,0]
	v_pk_mul_f32 v[146:147], v[146:147], v[2:3] op_sel_hi:[1,0]
	v_pk_mul_f32 v[144:145], v[144:145], v[2:3] op_sel_hi:[1,0]
	s_waitcnt lgkmcnt(4)
	v_mfma_f32_16x16x32_bf16 v[152:155], v[200:203], v[168:171], v[152:155]
	v_cvt_pk_bf16_f32 v188, v188, v189
	v_cvt_pk_bf16_f32 v189, v190, v191
	v_cvt_pk_bf16_f32 v190, v192, v193
	s_waitcnt lgkmcnt(2)
	v_mfma_f32_16x16x32_bf16 v[148:151], v[216:219], v[168:171], v[148:151]
	v_cvt_pk_bf16_f32 v191, v194, v195
	ds_read_b64_tr_b16 v[192:193], v221 offset:44288
	ds_read_b64_tr_b16 v[194:195], v221 offset:44800
	v_pk_add_f32 v[186:187], v[186:187], v[186:187] op_sel:[0,1] op_sel_hi:[1,0]
	s_waitcnt lgkmcnt(2)
	v_mfma_f32_16x16x32_bf16 v[144:147], v[196:199], v[168:171], v[144:147]
	ds_read_b64_tr_b16 v[168:169], v221 offset:46336
	ds_read_b64_tr_b16 v[170:171], v221 offset:46848
	v_cvt_scalef32_pk_bf16_fp8 v197, v58, 1.0 op_sel:[1,0,0]
	v_cvt_scalef32_pk_bf16_fp8 v196, v58, 1.0
	s_waitcnt lgkmcnt(2)
	v_mfma_f32_16x16x32_bf16 v[156:159], v[192:195], v[188:191], v[156:159]
	v_cvt_scalef32_pk_bf16_fp8 v198, v59, 1.0
	v_cvt_scalef32_pk_bf16_fp8 v199, v59, 1.0 op_sel:[1,0,0]
	s_waitcnt lgkmcnt(0)
	v_mfma_f32_16x16x32_bf16 v[152:155], v[168:171], v[188:191], v[152:155]
	ds_read_b64_tr_b16 v[168:169], v221 offset:48384
	ds_read_b64_tr_b16 v[170:171], v221 offset:48896
	ds_read_b64_tr_b16 v[192:193], v221 offset:50432
	ds_read_b64_tr_b16 v[194:195], v221 offset:50944
	s_waitcnt lgkmcnt(2)
	v_mfma_f32_16x16x32_bf16 v[148:151], v[168:171], v[188:191], v[148:151]
	v_cvt_scalef32_pk_bf16_fp8 v169, v56, 1.0 op_sel:[1,0,0]
	v_cvt_scalef32_pk_bf16_fp8 v168, v56, 1.0
	v_cvt_scalef32_pk_bf16_fp8 v171, v57, 1.0 op_sel:[1,0,0]
	v_cvt_scalef32_pk_bf16_fp8 v170, v57, 1.0
	ds_write_b128 v220, v[168:171] offset:43264
	ds_write_b128 v220, v[196:199] offset:43280
	v_cvt_scalef32_pk_bf16_fp8 v169, v52, 1.0 op_sel:[1,0,0]
	v_cvt_scalef32_pk_bf16_fp8 v168, v52, 1.0
	v_cvt_scalef32_pk_bf16_fp8 v171, v53, 1.0 op_sel:[1,0,0]
	v_cvt_scalef32_pk_bf16_fp8 v170, v53, 1.0
	v_cvt_scalef32_pk_bf16_fp8 v197, v54, 1.0 op_sel:[1,0,0]
	v_cvt_scalef32_pk_bf16_fp8 v196, v54, 1.0
	v_cvt_scalef32_pk_bf16_fp8 v198, v55, 1.0
	v_cvt_scalef32_pk_bf16_fp8 v199, v55, 1.0 op_sel:[1,0,0]
	ds_write_b128 v220, v[168:171] offset:43776
	ds_write_b128 v220, v[196:199] offset:43792
	s_waitcnt vmcnt(1)
	v_cvt_scalef32_pk_bf16_fp8 v169, v64, 1.0 op_sel:[1,0,0]
	v_cvt_scalef32_pk_bf16_fp8 v168, v64, 1.0
	v_cvt_scalef32_pk_bf16_fp8 v171, v65, 1.0 op_sel:[1,0,0]
	v_cvt_scalef32_pk_bf16_fp8 v170, v65, 1.0
	v_cvt_scalef32_pk_bf16_fp8 v197, v66, 1.0 op_sel:[1,0,0]
	v_cvt_scalef32_pk_bf16_fp8 v196, v66, 1.0
	v_cvt_scalef32_pk_bf16_fp8 v198, v67, 1.0
	v_cvt_scalef32_pk_bf16_fp8 v199, v67, 1.0 op_sel:[1,0,0]
	ds_write_b128 v220, v[168:171] offset:44288
	ds_write_b128 v220, v[196:199] offset:44304
	s_waitcnt vmcnt(0)
	v_cvt_scalef32_pk_bf16_fp8 v169, v60, 1.0 op_sel:[1,0,0]
	v_cvt_scalef32_pk_bf16_fp8 v168, v60, 1.0
	v_cvt_scalef32_pk_bf16_fp8 v171, v61, 1.0 op_sel:[1,0,0]
	v_cvt_scalef32_pk_bf16_fp8 v170, v61, 1.0
	v_cvt_scalef32_pk_bf16_fp8 v197, v62, 1.0 op_sel:[1,0,0]
	v_cvt_scalef32_pk_bf16_fp8 v196, v62, 1.0
	v_cvt_scalef32_pk_bf16_fp8 v198, v63, 1.0
	v_cvt_scalef32_pk_bf16_fp8 v199, v63, 1.0 op_sel:[1,0,0]
	ds_write_b128 v220, v[168:171] offset:44800
	ds_write_b128 v220, v[196:199] offset:44816
	v_cvt_pk_bf16_f32 v168, v178, v179
	v_cvt_pk_bf16_f32 v169, v180, v181
	v_cvt_pk_bf16_f32 v170, v182, v183
	v_cvt_pk_bf16_f32 v171, v184, v185
	ds_read_b64_tr_b16 v[178:179], v221 offset:43264
	ds_read_b64_tr_b16 v[180:181], v221 offset:43776
	ds_read_b64_tr_b16 v[182:183], v221 offset:45312
	ds_read_b64_tr_b16 v[184:185], v221 offset:45824
	s_waitcnt lgkmcnt(2)
	v_mfma_f32_16x16x32_bf16 v[156:159], v[178:181], v[168:171], v[156:159]
	s_waitcnt lgkmcnt(0)
	v_mfma_f32_16x16x32_bf16 v[152:155], v[182:185], v[168:171], v[152:155]
	ds_read_b64_tr_b16 v[178:179], v221 offset:47360
	ds_read_b64_tr_b16 v[180:181], v221 offset:47872
	ds_read_b64_tr_b16 v[182:183], v221 offset:49408
	ds_read_b64_tr_b16 v[184:185], v221 offset:49920
	v_mfma_f32_16x16x32_bf16 v[144:147], v[192:195], v[188:191], v[144:147]
	s_waitcnt lgkmcnt(2)
	v_mfma_f32_16x16x32_bf16 v[148:151], v[178:181], v[168:171], v[148:151]
	v_cvt_pk_bf16_f32 v178, v160, v161
	v_cvt_pk_bf16_f32 v179, v162, v163
	v_cvt_pk_bf16_f32 v180, v164, v165
	v_cvt_pk_bf16_f32 v181, v166, v167
	ds_read_b64_tr_b16 v[160:161], v221 offset:44288
	ds_read_b64_tr_b16 v[162:163], v221 offset:44800
	ds_read_b64_tr_b16 v[164:165], v221 offset:46336
	ds_read_b64_tr_b16 v[166:167], v221 offset:46848
	s_waitcnt lgkmcnt(4)
	v_mfma_f32_16x16x32_bf16 v[144:147], v[182:185], v[168:171], v[144:147]
	ds_read_b64_tr_b16 v[168:169], v221 offset:48384
	ds_read_b64_tr_b16 v[170:171], v221 offset:48896
	ds_read_b64_tr_b16 v[182:183], v221 offset:50432
	ds_read_b64_tr_b16 v[184:185], v221 offset:50944
	s_waitcnt lgkmcnt(6)
	v_mfma_f32_16x16x32_bf16 v[156:159], v[160:163], v[178:181], v[156:159]
	v_mov_b32_e32 v160, v186
	s_nop 1
	v_permlane16_swap_b32_e32 v186, v160
	s_waitcnt lgkmcnt(4)
	v_mfma_f32_16x16x32_bf16 v[152:155], v[164:167], v[178:181], v[152:155]
	v_add_f32_e32 v160, v186, v160
	v_mov_b32_e32 v161, v160
	s_nop 1
	v_permlane32_swap_b32_e32 v160, v161
	s_waitcnt lgkmcnt(2)
	v_mfma_f32_16x16x32_bf16 v[148:151], v[168:171], v[178:181], v[148:151]
	s_waitcnt lgkmcnt(0)
	v_mfma_f32_16x16x32_bf16 v[144:147], v[182:185], v[178:181], v[144:147]
	s_cbranch_vccnz .LBB0_1389
	v_mov_b64_e32 v[28:29], v[84:85]
	v_mov_b64_e32 v[32:33], v[88:89]
	v_mov_b64_e32 v[20:21], v[92:93]
	v_mov_b64_e32 v[24:25], v[96:97]
	v_mov_b64_e32 v[12:13], v[68:69]
	v_mov_b64_e32 v[16:17], v[72:73]
	v_mov_b64_e32 v[4:5], v[76:77]
	v_mov_b64_e32 v[8:9], v[80:81]
	v_mov_b64_e32 v[60:61], v[128:129]
	v_mov_b64_e32 v[64:65], v[104:105]
	v_mov_b64_e32 v[52:53], v[108:109]
	v_mov_b64_e32 v[56:57], v[112:113]
	v_mov_b64_e32 v[44:45], v[116:117]
	v_mov_b64_e32 v[48:49], v[120:121]
	v_mov_b64_e32 v[36:37], v[124:125]
	v_mov_b64_e32 v[40:41], v[100:101]
	v_mov_b64_e32 v[30:31], v[86:87]
	v_mov_b64_e32 v[34:35], v[90:91]
	v_mov_b64_e32 v[22:23], v[94:95]
	v_mov_b64_e32 v[26:27], v[98:99]
	v_mov_b64_e32 v[14:15], v[70:71]
	v_mov_b64_e32 v[18:19], v[74:75]
	v_mov_b64_e32 v[6:7], v[78:79]
	v_mov_b64_e32 v[10:11], v[82:83]
	v_mov_b64_e32 v[62:63], v[130:131]
	v_mov_b64_e32 v[66:67], v[106:107]
	v_mov_b64_e32 v[54:55], v[110:111]
	v_mov_b64_e32 v[58:59], v[114:115]
	v_mov_b64_e32 v[46:47], v[118:119]
	v_mov_b64_e32 v[50:51], v[122:123]
	v_mov_b64_e32 v[38:39], v[126:127]
	v_mov_b64_e32 v[42:43], v[102:103]
